# grid barrier: first arriver of each XCD starts an early L2 write-back so the leader's release write-back has less to flush
# baseline (speedup 1.0000x reference)
.LBB0_307:
	s_lshl_b32 s24, s33, 6
	s_add_i32 s6, s24, 0x500
	s_mov_b32 s7, 0
	s_lshl_b64 s[4:5], s[6:7], 2
	s_add_u32 s4, s36, s4
	s_addc_u32 s5, s37, s5
	v_mov_b32_e32 v1, 1
	v_mov_b64_e32 v[6:7], s[4:5]
	flat_atomic_add v1, v[6:7], v1 sc0
	v_cvt_f32_u32_e32 v3, v4
	v_sub_u32_e32 v5, 0, v4
	v_rcp_iflag_f32_e32 v3, v3
	s_nop 0
	v_mul_f32_e32 v3, 0x4f7ffffe, v3
	v_cvt_u32_f32_e32 v3, v3
	v_mul_lo_u32 v5, v5, v3
	v_mul_hi_u32 v5, v3, v5
	v_add_u32_e32 v3, v3, v5
	s_waitcnt vmcnt(0) lgkmcnt(0)
	buffer_inv sc1
	v_readfirstlane_b32 vcc_lo, v1
	s_and_b32 vcc_lo, vcc_lo, 31
	s_cmp_lg_u32 vcc_lo, 0
	s_cbranch_scc1 .Lxb_e0
	buffer_wbl2 sc1
.Lxb_e0:
	v_mul_hi_u32 v3, v1, v3
	v_mul_lo_u32 v5, v3, v4
	v_add_u32_e32 v6, 1, v1
	v_sub_u32_e32 v1, v1, v5
	v_add_u32_e32 v7, 1, v3
	v_cmp_ge_u32_e32 vcc, v1, v4
	v_sub_u32_e32 v5, v1, v4
	s_nop 0
	v_cndmask_b32_e32 v3, v3, v7, vcc
	v_cndmask_b32_e32 v1, v1, v5, vcc
	v_add_u32_e32 v5, 1, v3
	v_cmp_ge_u32_e32 vcc, v1, v4
	s_nop 1
	v_cndmask_b32_e32 v1, v3, v5, vcc
	v_mad_u64_u32 v[4:5], s[4:5], v4, v1, v[4:5]
	v_cmp_ne_u32_e32 vcc, v6, v4
	s_and_saveexec_b64 s[4:5], vcc
	s_xor_b64 s[4:5], exec, s[4:5]
	s_cbranch_execz .LBB0_320
	s_add_i32 s6, s24, 0x900
	s_lshl_b64 s[6:7], s[6:7], 2
	s_add_u32 s8, s36, s6
	s_addc_u32 s9, s37, s7
	v_mov_b64_e32 v[2:3], s[8:9]
	flat_load_dword v2, v[2:3] sc1
	s_waitcnt vmcnt(0) lgkmcnt(0)
	v_cmp_eq_u32_e32 vcc, v2, v1
	s_and_saveexec_b64 s[6:7], vcc
	s_cbranch_execz .LBB0_319
	s_mov_b32 s25, 1
	s_mov_b64 s[10:11], 0
	s_branch .LBB0_311

.LBB0_577:
	s_lshl_b32 s30, s42, 6
	s_add_i32 s48, s30, 0x500
	s_lshl_b64 s[10:11], s[48:49], 2
	s_add_u32 s10, s6, s10
	s_addc_u32 s11, s7, s11
	v_mov_b64_e32 v[6:7], s[10:11]
	flat_atomic_add v6, v[6:7], v232 sc0
	v_cvt_f32_u32_e32 v5, v4
	v_sub_u32_e32 v7, 0, v4
	v_rcp_iflag_f32_e32 v5, v5
	s_nop 0
	v_mul_f32_e32 v5, 0x4f7ffffe, v5
	v_cvt_u32_f32_e32 v5, v5
	v_mul_lo_u32 v7, v7, v5
	v_mul_hi_u32 v7, v5, v7
	v_add_u32_e32 v5, v5, v7
	s_waitcnt vmcnt(0) lgkmcnt(0)
	buffer_inv sc1
	v_readfirstlane_b32 vcc_lo, v6
	s_and_b32 vcc_lo, vcc_lo, 31
	s_cmp_lg_u32 vcc_lo, 0
	s_cbranch_scc1 .Lxb_e1
	buffer_wbl2 sc1
.Lxb_e1:
	v_mul_hi_u32 v5, v6, v5
	v_mul_lo_u32 v7, v5, v4
	v_sub_u32_e32 v7, v6, v7
	v_cmp_ge_u32_e32 vcc, v7, v4
	v_add_u32_e32 v8, 1, v5
	s_nop 0
	v_cndmask_b32_e32 v5, v5, v8, vcc
	v_sub_u32_e32 v8, v7, v4
	v_cndmask_b32_e32 v7, v7, v8, vcc
	v_cmp_ge_u32_e32 vcc, v7, v4
	v_add_u32_e32 v7, 1, v5
	v_add_u32_e32 v8, 1, v6
	v_cndmask_b32_e32 v5, v5, v7, vcc
	v_mad_u64_u32 v[6:7], s[10:11], v4, v5, v[4:5]
	v_cmp_ne_u32_e32 vcc, v8, v6
	s_and_saveexec_b64 s[10:11], vcc
	s_xor_b64 s[10:11], exec, s[10:11]
	s_cbranch_execz .LBB0_590
	s_add_i32 s48, s30, 0x900
	s_lshl_b64 s[12:13], s[48:49], 2
	s_add_u32 s14, s6, s12
	s_addc_u32 s15, s7, s13
	v_mov_b64_e32 v[6:7], s[14:15]
	flat_load_dword v2, v[6:7] sc1
	s_waitcnt vmcnt(0) lgkmcnt(0)
	v_cmp_eq_u32_e32 vcc, v2, v5
	s_and_saveexec_b64 s[12:13], vcc
	s_cbranch_execz .LBB0_589
	s_mov_b32 s31, 1
	s_mov_b64 s[16:17], 0
	s_branch .LBB0_581

.LBB0_1456:
	s_lshl_b32 s28, s42, 6
	s_add_i32 s48, s28, 0x500
	s_lshl_b64 s[6:7], s[48:49], 2
	s_add_u32 s6, s4, s6
	s_addc_u32 s7, s5, s7
	v_mov_b64_e32 v[6:7], s[6:7]
	flat_atomic_add v6, v[6:7], v232 sc0
	v_cvt_f32_u32_e32 v5, v4
	v_sub_u32_e32 v7, 0, v4
	v_rcp_iflag_f32_e32 v5, v5
	s_nop 0
	v_mul_f32_e32 v5, 0x4f7ffffe, v5
	v_cvt_u32_f32_e32 v5, v5
	v_mul_lo_u32 v7, v7, v5
	v_mul_hi_u32 v7, v5, v7
	v_add_u32_e32 v5, v5, v7
	s_waitcnt vmcnt(0) lgkmcnt(0)
	buffer_inv sc1
	v_readfirstlane_b32 vcc_lo, v6
	s_and_b32 vcc_lo, vcc_lo, 31
	s_cmp_lg_u32 vcc_lo, 0
	s_cbranch_scc1 .Lxb_e2
	buffer_wbl2 sc1
.Lxb_e2:
	v_mul_hi_u32 v5, v6, v5
	v_mul_lo_u32 v7, v5, v4
	v_sub_u32_e32 v7, v6, v7
	v_cmp_ge_u32_e32 vcc, v7, v4
	v_add_u32_e32 v8, 1, v5
	s_nop 0
	v_cndmask_b32_e32 v5, v5, v8, vcc
	v_sub_u32_e32 v8, v7, v4
	v_cndmask_b32_e32 v7, v7, v8, vcc
	v_cmp_ge_u32_e32 vcc, v7, v4
	v_add_u32_e32 v7, 1, v5
	v_add_u32_e32 v8, 1, v6
	v_cndmask_b32_e32 v5, v5, v7, vcc
	v_mad_u64_u32 v[6:7], s[6:7], v4, v5, v[4:5]
	v_cmp_ne_u32_e32 vcc, v8, v6
	s_and_saveexec_b64 s[6:7], vcc
	s_xor_b64 s[6:7], exec, s[6:7]
	s_cbranch_execz .LBB0_1469
	s_add_i32 s48, s28, 0x900
	s_lshl_b64 s[10:11], s[48:49], 2
	s_add_u32 s12, s4, s10
	s_addc_u32 s13, s5, s11
	v_mov_b64_e32 v[6:7], s[12:13]
	flat_load_dword v2, v[6:7] sc1
	s_waitcnt vmcnt(0) lgkmcnt(0)
	v_cmp_eq_u32_e32 vcc, v2, v5
	s_and_saveexec_b64 s[10:11], vcc
	s_cbranch_execz .LBB0_1468
	s_mov_b32 s29, 1
	s_mov_b64 s[14:15], 0
	s_branch .LBB0_1460

.LBB0_1946:
	s_lshl_b32 s28, s33, 6
	s_add_i32 s48, s28, 0x500
	s_lshl_b64 s[6:7], s[48:49], 2
	s_add_u32 s6, s4, s6
	s_addc_u32 s7, s5, s7
	v_mov_b64_e32 v[6:7], s[6:7]
	flat_atomic_add v6, v[6:7], v232 sc0
	v_cvt_f32_u32_e32 v5, v4
	v_sub_u32_e32 v7, 0, v4
	v_rcp_iflag_f32_e32 v5, v5
	s_nop 0
	v_mul_f32_e32 v5, 0x4f7ffffe, v5
	v_cvt_u32_f32_e32 v5, v5
	v_mul_lo_u32 v7, v7, v5
	v_mul_hi_u32 v7, v5, v7
	v_add_u32_e32 v5, v5, v7
	s_waitcnt vmcnt(0) lgkmcnt(0)
	buffer_inv sc1
	v_readfirstlane_b32 vcc_lo, v6
	s_and_b32 vcc_lo, vcc_lo, 31
	s_cmp_lg_u32 vcc_lo, 0
	s_cbranch_scc1 .Lxb_e3
	buffer_wbl2 sc1

.LBB0_2125:
	s_lshl_b32 s30, s42, 6
	s_add_i32 s48, s30, 0x500
	s_lshl_b64 s[10:11], s[48:49], 2
	s_add_u32 s10, s4, s10
	s_addc_u32 s11, s5, s11
	v_mov_b64_e32 v[6:7], s[10:11]
	flat_atomic_add v6, v[6:7], v232 sc0
	v_cvt_f32_u32_e32 v5, v4
	v_sub_u32_e32 v7, 0, v4
	v_rcp_iflag_f32_e32 v5, v5
	s_nop 0
	v_mul_f32_e32 v5, 0x4f7ffffe, v5
	v_cvt_u32_f32_e32 v5, v5
	v_mul_lo_u32 v7, v7, v5
	v_mul_hi_u32 v7, v5, v7
	v_add_u32_e32 v5, v5, v7
	s_waitcnt vmcnt(0) lgkmcnt(0)
	buffer_inv sc1
	v_readfirstlane_b32 vcc_lo, v6
	s_and_b32 vcc_lo, vcc_lo, 31
	s_cmp_lg_u32 vcc_lo, 0
	s_cbranch_scc1 .Lxb_e4
	buffer_wbl2 sc1
.Lxb_e4:
	v_mul_hi_u32 v5, v6, v5
	v_mul_lo_u32 v7, v5, v4
	v_sub_u32_e32 v7, v6, v7
	v_cmp_ge_u32_e32 vcc, v7, v4
	v_add_u32_e32 v8, 1, v5
	s_nop 0
	v_cndmask_b32_e32 v5, v5, v8, vcc
	v_sub_u32_e32 v8, v7, v4
	v_cndmask_b32_e32 v7, v7, v8, vcc
	v_cmp_ge_u32_e32 vcc, v7, v4
	v_add_u32_e32 v7, 1, v5
	v_add_u32_e32 v8, 1, v6
	v_cndmask_b32_e32 v5, v5, v7, vcc
	v_mad_u64_u32 v[6:7], s[10:11], v4, v5, v[4:5]
	v_cmp_ne_u32_e32 vcc, v8, v6
	s_and_saveexec_b64 s[10:11], vcc
	s_xor_b64 s[10:11], exec, s[10:11]
	s_cbranch_execz .LBB0_2138
	s_add_i32 s48, s30, 0x900
	s_lshl_b64 s[12:13], s[48:49], 2
	s_add_u32 s14, s4, s12
	s_addc_u32 s15, s5, s13
	v_mov_b64_e32 v[6:7], s[14:15]
	flat_load_dword v2, v[6:7] sc1
	s_waitcnt vmcnt(0) lgkmcnt(0)
	v_cmp_eq_u32_e32 vcc, v2, v5
	s_and_saveexec_b64 s[12:13], vcc
	s_cbranch_execz .LBB0_2137
	s_mov_b32 s31, 1
	s_mov_b64 s[16:17], 0
	s_branch .LBB0_2129

.LBB0_2279:
	s_lshl_b32 s30, s43, 6
	s_add_i32 s48, s30, 0x500
	s_lshl_b64 s[10:11], s[48:49], 2
	s_add_u32 s10, s6, s10
	s_addc_u32 s11, s7, s11
	v_mov_b64_e32 v[6:7], s[10:11]
	flat_atomic_add v6, v[6:7], v232 sc0
	v_cvt_f32_u32_e32 v5, v4
	v_sub_u32_e32 v7, 0, v4
	v_rcp_iflag_f32_e32 v5, v5
	s_nop 0
	v_mul_f32_e32 v5, 0x4f7ffffe, v5
	v_cvt_u32_f32_e32 v5, v5
	v_mul_lo_u32 v7, v7, v5
	v_mul_hi_u32 v7, v5, v7
	v_add_u32_e32 v5, v5, v7
	s_waitcnt vmcnt(0) lgkmcnt(0)
	buffer_inv sc1
	v_readfirstlane_b32 vcc_lo, v6
	s_and_b32 vcc_lo, vcc_lo, 31
	s_cmp_lg_u32 vcc_lo, 0
	s_cbranch_scc1 .Lxb_e6
	buffer_wbl2 sc1

.LBB0_2400:
	s_lshl_b32 s30, s33, 6
	s_add_i32 s48, s30, 0x500
	s_lshl_b64 s[10:11], s[48:49], 2
	s_add_u32 s10, s6, s10
	s_addc_u32 s11, s7, s11
	v_mov_b64_e32 v[6:7], s[10:11]
	flat_atomic_add v6, v[6:7], v232 sc0
	v_cvt_f32_u32_e32 v5, v4
	v_sub_u32_e32 v7, 0, v4
	v_rcp_iflag_f32_e32 v5, v5
	s_nop 0
	v_mul_f32_e32 v5, 0x4f7ffffe, v5
	v_cvt_u32_f32_e32 v5, v5
	v_mul_lo_u32 v7, v7, v5
	v_mul_hi_u32 v7, v5, v7
	v_add_u32_e32 v5, v5, v7
	s_waitcnt vmcnt(0) lgkmcnt(0)
	buffer_inv sc1
	v_readfirstlane_b32 vcc_lo, v6
	s_and_b32 vcc_lo, vcc_lo, 31
	s_cmp_lg_u32 vcc_lo, 0
	s_cbranch_scc1 .Lxb_e7
	buffer_wbl2 sc1
